# DPP / permlane instead of LDS round trips, part 3: 12 lane^16 / lane^32 all-reduce steps in the odd-layer c-norm pass use v_mov + v_permlane16/32_swap (same addends) instead of ds_bpermute
# speedup vs baseline: 1.0012x; 1.0012x over previous
; __device__ __forceinline__ void odd_c_phase(Frame& F, KArgs a, int j) {
;     ...
;             const int r = rw[k]; const int b = r / TPS, t = r - b * TPS; const bool lat = t < SEQ;
;             const float sq = wave_sum((cq[k][0] * cq[k][0] + cq[k][1] * cq[k][1]) + (cq[k][2] * cq[k][2] + cq[k][3] * cq[k][3]));
;             const float skv = wave_sum(ckv[k][0] * ckv[k][0] + ckv[k][1] * ckv[k][1]);
;             const float skr = wave_sum(kr[k] * kr[k]);
;             const float rq = rsqrtf(sq * (1.f / 256.f) + EPS), rkv = rsqrtf(skv * (1.f / 128.f) + EPS), rkr = rsqrtf(skr * (1.f / 32.f) + EPS);
;             bf16_t* cn = CN + (size_t)r * CNW;
;             float kv = kr[k] * rkr * gkr;
;             const float partner = __shfl_xor(kv, 8);
;             if (lat) { const int pos = (lane & 16) ? (t & 63) : (t >> 6); const f32x2 cs = R32[pos * 8 + (lane & 7)];
;                 kv = (lane & 8) ? (kv * cs.x + partner * cs.y) : (kv * cs.x - partner * cs.y); }
.LBB0_397:
	s_or_b64 exec, exec, s[14:15]
	s_waitcnt vmcnt(7)
	v_pk_mul_f32 v[38:39], v[20:21], v[20:21]
	v_pk_mul_f32 v[52:53], v[18:19], v[18:19]
	v_mov_b32_e32 v55, v39
	v_mov_b32_e32 v54, v52
	v_pk_mov_b32 v[38:39], v[52:53], v[38:39] op_sel:[1,0]
	s_waitcnt vmcnt(6)
	v_mul_f32_e32 v56, v51, v51
	v_pk_add_f32 v[38:39], v[38:39], v[54:55]
	s_nop 1
	v_mov_b32_dpp v54, v56 quad_perm:[1,0,3,2] row_mask:0xf bank_mask:0xf
	v_add_f32_e32 v38, v38, v39
	s_nop 1
	v_mov_b32_dpp v39, v38 quad_perm:[1,0,3,2] row_mask:0xf bank_mask:0xf
	s_mul_hi_i32 s10, s22, 0x3e0f83e1
	s_lshr_b32 s11, s10, 31
	s_ashr_i32 s10, s10, 11
	s_add_i32 s10, s10, s11
	s_waitcnt lgkmcnt(0)
	v_add_f32_e32 v38, v38, v39
	s_nop 1
	v_mov_b32_dpp v39, v38 quad_perm:[2,3,0,1] row_mask:0xf bank_mask:0xf
	s_mulk_i32 s10, 0x2100
	s_sub_i32 s14, s22, s10
	s_mov_b32 s10, 0x3d000000
	s_brev_b32 s11, 60
	s_waitcnt lgkmcnt(0)
	v_add_f32_e32 v38, v38, v39
	s_nop 1
	v_mov_b32_dpp v39, v38 row_shl:4 row_mask:0xf bank_mask:0x5
	v_mov_b32_dpp v39, v38 row_shr:4 row_mask:0xf bank_mask:0xa
	s_cmpk_gt_i32 s14, 0x1fff
	s_waitcnt lgkmcnt(0)
	v_add_f32_e32 v38, v38, v39
	s_nop 1
	v_mov_b32_dpp v39, v38 row_shl:8 row_mask:0xf bank_mask:0x3
	v_mov_b32_dpp v39, v38 row_shr:8 row_mask:0xf bank_mask:0xc
	s_waitcnt lgkmcnt(0)
	v_add_f32_e32 v38, v38, v39
	ds_bpermute_b32 v39, v43, v38
	s_waitcnt lgkmcnt(0)
	v_add_f32_e32 v52, v38, v39
	v_mul_f32_e32 v38, v37, v37
	v_pk_fma_f32 v[38:39], v[36:37], v[36:37], v[38:39] op_sel_hi:[1,1,0]
	s_nop 1
	v_mov_b32_dpp v55, v38 quad_perm:[1,0,3,2] row_mask:0xf bank_mask:0xf
	v_mov_b32_e32 v57, v38
	ds_bpermute_b32 v53, v44, v52
	s_waitcnt lgkmcnt(0)
	v_pk_add_f32 v[38:39], v[56:57], v[54:55]
	s_nop 1
	v_mov_b32_dpp v55, v39 quad_perm:[2,3,0,1] row_mask:0xf bank_mask:0xf
	s_nop 1
	v_mov_b32_dpp v54, v38 quad_perm:[2,3,0,1] row_mask:0xf bank_mask:0xf
	s_waitcnt lgkmcnt(0)
	v_pk_add_f32 v[38:39], v[38:39], v[54:55]
	s_nop 1
	v_mov_b32_dpp v55, v39 row_shl:4 row_mask:0xf bank_mask:0x5
	v_mov_b32_dpp v55, v39 row_shr:4 row_mask:0xf bank_mask:0xa
	s_nop 1
	v_mov_b32_dpp v54, v38 row_shl:4 row_mask:0xf bank_mask:0x5
	v_mov_b32_dpp v54, v38 row_shr:4 row_mask:0xf bank_mask:0xa
	s_waitcnt lgkmcnt(0)
	v_pk_add_f32 v[38:39], v[38:39], v[54:55]
	s_nop 1
	v_mov_b32_dpp v55, v39 row_shl:8 row_mask:0xf bank_mask:0x3
	v_mov_b32_dpp v55, v39 row_shr:8 row_mask:0xf bank_mask:0xc
	s_nop 1
	v_mov_b32_dpp v54, v38 row_shl:8 row_mask:0xf bank_mask:0x3
	v_mov_b32_dpp v54, v38 row_shr:8 row_mask:0xf bank_mask:0xc
	s_waitcnt lgkmcnt(0)
	v_pk_add_f32 v[38:39], v[38:39], v[54:55]
	v_mov_b32_e32 v55, v39
	s_nop 1
	v_permlane16_swap_b32_e32 v39, v55
	v_mov_b32_e32 v54, v38
	s_nop 1
	v_permlane16_swap_b32_e32 v38, v54
	s_waitcnt lgkmcnt(0)
	v_pk_add_f32 v[38:39], v[38:39], v[54:55]
	ds_bpermute_b32 v55, v44, v39
	v_mov_b32_e32 v54, v38
	s_nop 1
	v_permlane32_swap_b32_e32 v38, v54
	s_waitcnt lgkmcnt(0)
	v_pk_add_f32 v[38:39], v[38:39], v[54:55]
	s_nop 0
	v_pk_fma_f32 v[38:39], v[38:39], s[10:11], v[196:197] op_sel_hi:[1,1,0]
	s_nop 0
	v_cmp_gt_f32_e64 s[10:11], s95, v38
	v_mul_f32_e32 v54, 0x4b800000, v38
	v_cmp_gt_f32_e32 vcc, s95, v39
	v_cndmask_b32_e64 v38, v38, v54, s[10:11]
	v_rsq_f32_e32 v38, v38
	s_nop 0
	v_mul_f32_e32 v54, 0x45800000, v38
	v_cndmask_b32_e64 v38, v38, v54, s[10:11]
	v_mul_f32_e32 v38, v51, v38
	v_mul_f32_e32 v38, v23, v38
	s_nop 1
	v_mov_b32_dpp v51, v38 row_shl:8 row_mask:0xf bank_mask:0x3
	v_mov_b32_dpp v51, v38 row_shr:8 row_mask:0xf bank_mask:0xc
	s_cbranch_scc1 .LBB0_399
	s_and_b32 s10, s14, 63
	s_ashr_i32 s11, s14, 6
	v_mov_b32_e32 v54, s10
	v_mov_b32_e32 v55, s11
	v_cndmask_b32_e64 v54, v54, v55, s[6:7]
	v_lshl_or_b32 v54, v54, 3, v46
	v_ashrrev_i32_e32 v55, 31, v54
	v_lshl_add_u64 v[54:55], v[54:55], 3, s[26:27]
	global_load_dwordx2 v[54:55], v[54:55], off
	s_waitcnt vmcnt(0) lgkmcnt(0)
	v_mul_f32_e32 v51, v55, v51
	v_cndmask_b32_e64 v51, v51, -v51, s[8:9]
	v_fmac_f32_e32 v51, v38, v54
	v_mov_b32_e32 v38, v51

; __device__ __forceinline__ void odd_c_phase(Frame& F, KArgs a, int j) {
;     ...
;             const int r = rw[k]; const int b = r / TPS, t = r - b * TPS; const bool lat = t < SEQ;
;             const float sq = wave_sum((cq[k][0] * cq[k][0] + cq[k][1] * cq[k][1]) + (cq[k][2] * cq[k][2] + cq[k][3] * cq[k][3]));
;             const float skv = wave_sum(ckv[k][0] * ckv[k][0] + ckv[k][1] * ckv[k][1]);
;             const float skr = wave_sum(kr[k] * kr[k]);
;             const float rq = rsqrtf(sq * (1.f / 256.f) + EPS), rkv = rsqrtf(skv * (1.f / 128.f) + EPS), rkr = rsqrtf(skr * (1.f / 32.f) + EPS);
;             bf16_t* cn = CN + (size_t)r * CNW;
;             float kv = kr[k] * rkr * gkr;
;             const float partner = __shfl_xor(kv, 8);
;             if (lat) { const int pos = (lane & 16) ? (t & 63) : (t >> 6); const f32x2 cs = R32[pos * 8 + (lane & 7)];
;                 kv = (lane & 8) ? (kv * cs.x + partner * cs.y) : (kv * cs.x - partner * cs.y); }
.LBB0_401:
	s_or_b64 exec, exec, s[10:11]
	s_waitcnt vmcnt(8)
	v_pk_mul_f32 v[18:19], v[16:17], v[16:17]
	v_pk_mul_f32 v[36:37], v[14:15], v[14:15]
	s_waitcnt lgkmcnt(0)
	v_mov_b32_e32 v39, v19
	v_mov_b32_e32 v38, v36
	v_pk_mov_b32 v[18:19], v[36:37], v[18:19] op_sel:[1,0]
	s_waitcnt vmcnt(7)
	v_mul_f32_e32 v52, v50, v50
	v_pk_add_f32 v[18:19], v[18:19], v[38:39]
	s_nop 1
	v_mov_b32_dpp v38, v52 quad_perm:[1,0,3,2] row_mask:0xf bank_mask:0xf
	v_add_f32_e32 v18, v18, v19
	s_nop 1
	v_mov_b32_dpp v19, v18 quad_perm:[1,0,3,2] row_mask:0xf bank_mask:0xf
	s_mul_hi_i32 s10, s50, 0x3e0f83e1
	s_lshr_b32 s11, s10, 31
	s_ashr_i32 s10, s10, 11
	s_add_i32 s10, s10, s11
	s_waitcnt lgkmcnt(0)
	v_add_f32_e32 v18, v18, v19
	s_nop 1
	v_mov_b32_dpp v19, v18 quad_perm:[2,3,0,1] row_mask:0xf bank_mask:0xf
	s_mulk_i32 s10, 0x2100
	s_sub_i32 s14, s50, s10
	s_mov_b32 s10, 0x3d000000
	s_brev_b32 s11, 60
	s_waitcnt lgkmcnt(0)
	v_add_f32_e32 v18, v18, v19
	s_nop 1
	v_mov_b32_dpp v19, v18 row_shl:4 row_mask:0xf bank_mask:0x5
	v_mov_b32_dpp v19, v18 row_shr:4 row_mask:0xf bank_mask:0xa
	s_cmpk_gt_i32 s14, 0x1fff
	s_waitcnt lgkmcnt(0)
	v_add_f32_e32 v18, v18, v19
	s_nop 1
	v_mov_b32_dpp v19, v18 row_shl:8 row_mask:0xf bank_mask:0x3
	v_mov_b32_dpp v19, v18 row_shr:8 row_mask:0xf bank_mask:0xc
	s_waitcnt lgkmcnt(0)
	v_add_f32_e32 v18, v18, v19
	ds_bpermute_b32 v19, v43, v18
	s_waitcnt lgkmcnt(0)
	v_add_f32_e32 v36, v18, v19
	v_mul_f32_e32 v18, v35, v35
	v_pk_fma_f32 v[18:19], v[34:35], v[34:35], v[18:19] op_sel_hi:[1,1,0]
	s_nop 1
	v_mov_b32_dpp v39, v18 quad_perm:[1,0,3,2] row_mask:0xf bank_mask:0xf
	v_mov_b32_e32 v53, v18
	ds_bpermute_b32 v37, v44, v36
	s_waitcnt lgkmcnt(0)
	v_pk_add_f32 v[18:19], v[52:53], v[38:39]
	s_nop 1
	v_mov_b32_dpp v39, v19 quad_perm:[2,3,0,1] row_mask:0xf bank_mask:0xf
	s_nop 1
	v_mov_b32_dpp v38, v18 quad_perm:[2,3,0,1] row_mask:0xf bank_mask:0xf
	s_waitcnt lgkmcnt(0)
	v_pk_add_f32 v[18:19], v[18:19], v[38:39]
	s_nop 1
	v_mov_b32_dpp v39, v19 row_shl:4 row_mask:0xf bank_mask:0x5
	v_mov_b32_dpp v39, v19 row_shr:4 row_mask:0xf bank_mask:0xa
	s_nop 1
	v_mov_b32_dpp v38, v18 row_shl:4 row_mask:0xf bank_mask:0x5
	v_mov_b32_dpp v38, v18 row_shr:4 row_mask:0xf bank_mask:0xa
	s_waitcnt lgkmcnt(0)
	v_pk_add_f32 v[18:19], v[18:19], v[38:39]
	s_nop 1
	v_mov_b32_dpp v39, v19 row_shl:8 row_mask:0xf bank_mask:0x3
	v_mov_b32_dpp v39, v19 row_shr:8 row_mask:0xf bank_mask:0xc
	s_nop 1
	v_mov_b32_dpp v38, v18 row_shl:8 row_mask:0xf bank_mask:0x3
	v_mov_b32_dpp v38, v18 row_shr:8 row_mask:0xf bank_mask:0xc
	s_waitcnt lgkmcnt(0)
	v_pk_add_f32 v[18:19], v[18:19], v[38:39]
	v_mov_b32_e32 v39, v19
	s_nop 1
	v_permlane16_swap_b32_e32 v19, v39
	v_mov_b32_e32 v38, v18
	s_nop 1
	v_permlane16_swap_b32_e32 v18, v38
	s_waitcnt lgkmcnt(0)
	v_pk_add_f32 v[18:19], v[18:19], v[38:39]
	ds_bpermute_b32 v39, v44, v19
	v_mov_b32_e32 v38, v18
	s_nop 1
	v_permlane32_swap_b32_e32 v18, v38
	s_waitcnt lgkmcnt(0)
	v_pk_add_f32 v[18:19], v[18:19], v[38:39]
	s_nop 0
	v_pk_fma_f32 v[18:19], v[18:19], s[10:11], v[196:197] op_sel_hi:[1,1,0]
	s_nop 0
	v_cmp_gt_f32_e32 vcc, s95, v18
	v_mul_f32_e32 v38, 0x4b800000, v18
	v_cmp_gt_f32_e64 s[10:11], s95, v19
	v_cndmask_b32_e32 v18, v18, v38, vcc
	v_rsq_f32_e32 v18, v18
	s_nop 0
	v_mul_f32_e32 v38, 0x45800000, v18
	v_cndmask_b32_e32 v18, v18, v38, vcc
	v_mul_f32_e32 v18, v50, v18
	v_mul_f32_e32 v18, v23, v18
	s_nop 1
	v_mov_b32_dpp v38, v18 row_shl:8 row_mask:0xf bank_mask:0x3
	v_mov_b32_dpp v38, v18 row_shr:8 row_mask:0xf bank_mask:0xc
	s_cbranch_scc1 .LBB0_403
	s_and_b32 s15, s14, 63
	s_ashr_i32 s14, s14, 6
	v_mov_b32_e32 v39, s15
	v_mov_b32_e32 v50, s14
	v_cndmask_b32_e64 v39, v39, v50, s[6:7]
	v_lshl_or_b32 v50, v39, 3, v46
	v_ashrrev_i32_e32 v51, 31, v50
	v_lshl_add_u64 v[50:51], v[50:51], 3, s[26:27]
	global_load_dwordx2 v[50:51], v[50:51], off
	s_waitcnt vmcnt(0) lgkmcnt(0)
	v_mul_f32_e32 v38, v51, v38
	v_cndmask_b32_e64 v38, v38, -v38, s[8:9]
	v_fmac_f32_e32 v38, v18, v50
	v_mov_b32_e32 v18, v38

; __device__ __forceinline__ void odd_c_phase(Frame& F, KArgs a, int j) {
;     ...
;             const int r = rw[k]; const int b = r / TPS, t = r - b * TPS; const bool lat = t < SEQ;
;             const float sq = wave_sum((cq[k][0] * cq[k][0] + cq[k][1] * cq[k][1]) + (cq[k][2] * cq[k][2] + cq[k][3] * cq[k][3]));
;             const float skv = wave_sum(ckv[k][0] * ckv[k][0] + ckv[k][1] * ckv[k][1]);
;             const float skr = wave_sum(kr[k] * kr[k]);
;             const float rq = rsqrtf(sq * (1.f / 256.f) + EPS), rkv = rsqrtf(skv * (1.f / 128.f) + EPS), rkr = rsqrtf(skr * (1.f / 32.f) + EPS);
;             bf16_t* cn = CN + (size_t)r * CNW;
;             float kv = kr[k] * rkr * gkr;
;             const float partner = __shfl_xor(kv, 8);
;             if (lat) { const int pos = (lane & 16) ? (t & 63) : (t >> 6); const f32x2 cs = R32[pos * 8 + (lane & 7)];
;                 kv = (lane & 8) ? (kv * cs.x + partner * cs.y) : (kv * cs.x - partner * cs.y); }
.LBB0_407:
	s_waitcnt vmcnt(6)
	v_pk_mul_f32 v[14:15], v[12:13], v[12:13]
	v_pk_mul_f32 v[16:17], v[10:11], v[10:11]
	v_mov_b32_e32 v19, v15
	v_mov_b32_e32 v18, v16
	v_pk_mov_b32 v[14:15], v[16:17], v[14:15] op_sel:[1,0]
	s_waitcnt vmcnt(5)
	v_mul_f32_e32 v34, v49, v49
	v_pk_add_f32 v[14:15], v[14:15], v[18:19]
	s_nop 1
	v_mov_b32_dpp v18, v34 quad_perm:[1,0,3,2] row_mask:0xf bank_mask:0xf
	v_add_f32_e32 v14, v14, v15
	s_nop 1
	v_mov_b32_dpp v15, v14 quad_perm:[1,0,3,2] row_mask:0xf bank_mask:0xf
	s_mul_hi_i32 s10, s44, 0x3e0f83e1
	s_lshr_b32 s11, s10, 31
	s_ashr_i32 s10, s10, 11
	s_add_i32 s10, s10, s11
	s_waitcnt lgkmcnt(0)
	v_add_f32_e32 v14, v14, v15
	s_nop 1
	v_mov_b32_dpp v15, v14 quad_perm:[2,3,0,1] row_mask:0xf bank_mask:0xf
	s_mulk_i32 s10, 0x2100
	s_sub_i32 s14, s44, s10
	s_mov_b32 s10, 0x3d000000
	s_brev_b32 s11, 60
	s_waitcnt lgkmcnt(0)
	v_add_f32_e32 v14, v14, v15
	s_nop 1
	v_mov_b32_dpp v15, v14 row_shl:4 row_mask:0xf bank_mask:0x5
	v_mov_b32_dpp v15, v14 row_shr:4 row_mask:0xf bank_mask:0xa
	s_cmpk_gt_i32 s14, 0x1fff
	s_waitcnt lgkmcnt(0)
	v_add_f32_e32 v14, v14, v15
	s_nop 1
	v_mov_b32_dpp v15, v14 row_shl:8 row_mask:0xf bank_mask:0x3
	v_mov_b32_dpp v15, v14 row_shr:8 row_mask:0xf bank_mask:0xc
	s_waitcnt lgkmcnt(0)
	v_add_f32_e32 v14, v14, v15
	ds_bpermute_b32 v15, v43, v14
	s_waitcnt lgkmcnt(0)
	v_add_f32_e32 v16, v14, v15
	v_mul_f32_e32 v14, v33, v33
	v_pk_fma_f32 v[14:15], v[32:33], v[32:33], v[14:15] op_sel_hi:[1,1,0]
	s_nop 1
	v_mov_b32_dpp v19, v14 quad_perm:[1,0,3,2] row_mask:0xf bank_mask:0xf
	v_mov_b32_e32 v35, v14
	ds_bpermute_b32 v17, v44, v16
	s_waitcnt lgkmcnt(0)
	v_pk_add_f32 v[14:15], v[34:35], v[18:19]
	s_nop 1
	v_mov_b32_dpp v19, v15 quad_perm:[2,3,0,1] row_mask:0xf bank_mask:0xf
	s_nop 1
	v_mov_b32_dpp v18, v14 quad_perm:[2,3,0,1] row_mask:0xf bank_mask:0xf
	s_waitcnt lgkmcnt(0)
	v_pk_add_f32 v[14:15], v[14:15], v[18:19]
	s_nop 1
	v_mov_b32_dpp v19, v15 row_shl:4 row_mask:0xf bank_mask:0x5
	v_mov_b32_dpp v19, v15 row_shr:4 row_mask:0xf bank_mask:0xa
	s_nop 1
	v_mov_b32_dpp v18, v14 row_shl:4 row_mask:0xf bank_mask:0x5
	v_mov_b32_dpp v18, v14 row_shr:4 row_mask:0xf bank_mask:0xa
	s_waitcnt lgkmcnt(0)
	v_pk_add_f32 v[14:15], v[14:15], v[18:19]
	s_nop 1
	v_mov_b32_dpp v19, v15 row_shl:8 row_mask:0xf bank_mask:0x3
	v_mov_b32_dpp v19, v15 row_shr:8 row_mask:0xf bank_mask:0xc
	s_nop 1
	v_mov_b32_dpp v18, v14 row_shl:8 row_mask:0xf bank_mask:0x3
	v_mov_b32_dpp v18, v14 row_shr:8 row_mask:0xf bank_mask:0xc
	s_waitcnt lgkmcnt(0)
	v_pk_add_f32 v[14:15], v[14:15], v[18:19]
	v_mov_b32_e32 v19, v15
	s_nop 1
	v_permlane16_swap_b32_e32 v15, v19
	v_mov_b32_e32 v18, v14
	s_nop 1
	v_permlane16_swap_b32_e32 v14, v18
	s_waitcnt lgkmcnt(0)
	v_pk_add_f32 v[14:15], v[14:15], v[18:19]
	ds_bpermute_b32 v19, v44, v15
	v_mov_b32_e32 v18, v14
	s_nop 1
	v_permlane32_swap_b32_e32 v14, v18
	s_waitcnt lgkmcnt(0)
	v_pk_add_f32 v[14:15], v[14:15], v[18:19]
	s_nop 0
	v_pk_fma_f32 v[14:15], v[14:15], s[10:11], v[196:197] op_sel_hi:[1,1,0]
	s_nop 0
	v_cmp_gt_f32_e32 vcc, s95, v14
	v_mul_f32_e32 v18, 0x4b800000, v14
	v_cmp_gt_f32_e64 s[10:11], s95, v15
	v_cndmask_b32_e32 v14, v14, v18, vcc
	v_rsq_f32_e32 v14, v14
	s_nop 0
	v_mul_f32_e32 v18, 0x45800000, v14
	v_cndmask_b32_e32 v14, v14, v18, vcc
	v_mul_f32_e32 v14, v49, v14
	v_mul_f32_e32 v14, v23, v14
	s_nop 1
	v_mov_b32_dpp v18, v14 row_shl:8 row_mask:0xf bank_mask:0x3
	v_mov_b32_dpp v18, v14 row_shr:8 row_mask:0xf bank_mask:0xc
	s_cbranch_scc1 .LBB0_409
	s_and_b32 s15, s14, 63
	s_ashr_i32 s14, s14, 6
	v_mov_b32_e32 v19, s15
	v_mov_b32_e32 v34, s14
	v_cndmask_b32_e64 v19, v19, v34, s[6:7]
	v_lshl_or_b32 v34, v19, 3, v46
	v_ashrrev_i32_e32 v35, 31, v34
	v_lshl_add_u64 v[34:35], v[34:35], 3, s[26:27]
	global_load_dwordx2 v[34:35], v[34:35], off
	s_waitcnt vmcnt(0) lgkmcnt(0)
	v_mul_f32_e32 v18, v35, v18
	v_cndmask_b32_e64 v18, v18, -v18, s[8:9]
	v_fmac_f32_e32 v18, v14, v34
	v_mov_b32_e32 v14, v18

; __device__ __forceinline__ void odd_c_phase(Frame& F, KArgs a, int j) {
;     ...
;             const int r = rw[k]; const int b = r / TPS, t = r - b * TPS; const bool lat = t < SEQ;
;             const float sq = wave_sum((cq[k][0] * cq[k][0] + cq[k][1] * cq[k][1]) + (cq[k][2] * cq[k][2] + cq[k][3] * cq[k][3]));
;             const float skv = wave_sum(ckv[k][0] * ckv[k][0] + ckv[k][1] * ckv[k][1]);
;             const float skr = wave_sum(kr[k] * kr[k]);
;             const float rq = rsqrtf(sq * (1.f / 256.f) + EPS), rkv = rsqrtf(skv * (1.f / 128.f) + EPS), rkr = rsqrtf(skr * (1.f / 32.f) + EPS);
;             bf16_t* cn = CN + (size_t)r * CNW;
;             float kv = kr[k] * rkr * gkr;
;             const float partner = __shfl_xor(kv, 8);
;             if (lat) { const int pos = (lane & 16) ? (t & 63) : (t >> 6); const f32x2 cs = R32[pos * 8 + (lane & 7)];
;                 kv = (lane & 8) ? (kv * cs.x + partner * cs.y) : (kv * cs.x - partner * cs.y); }
.LBB0_413:
	s_waitcnt vmcnt(4)
	v_pk_mul_f32 v[10:11], v[8:9], v[8:9]
	v_pk_mul_f32 v[12:13], v[6:7], v[6:7]
	v_mov_b32_e32 v15, v11
	v_mov_b32_e32 v14, v12
	v_pk_mov_b32 v[10:11], v[12:13], v[10:11] op_sel:[1,0]
	s_waitcnt vmcnt(3)
	v_mul_f32_e32 v16, v48, v48
	v_pk_add_f32 v[10:11], v[10:11], v[14:15]
	s_nop 1
	v_mov_b32_dpp v14, v16 quad_perm:[1,0,3,2] row_mask:0xf bank_mask:0xf
	v_add_f32_e32 v10, v10, v11
	s_nop 1
	v_mov_b32_dpp v11, v10 quad_perm:[1,0,3,2] row_mask:0xf bank_mask:0xf
	s_mul_hi_i32 s10, s36, 0x3e0f83e1
	s_lshr_b32 s11, s10, 31
	s_ashr_i32 s10, s10, 11
	s_add_i32 s10, s10, s11
	s_waitcnt lgkmcnt(0)
	v_add_f32_e32 v10, v10, v11
	s_nop 1
	v_mov_b32_dpp v11, v10 quad_perm:[2,3,0,1] row_mask:0xf bank_mask:0xf
	s_mulk_i32 s10, 0x2100
	s_sub_i32 s14, s36, s10
	s_mov_b32 s10, 0x3d000000
	s_brev_b32 s11, 60
	s_waitcnt lgkmcnt(0)
	v_add_f32_e32 v10, v10, v11
	s_nop 1
	v_mov_b32_dpp v11, v10 row_shl:4 row_mask:0xf bank_mask:0x5
	v_mov_b32_dpp v11, v10 row_shr:4 row_mask:0xf bank_mask:0xa
	s_cmpk_gt_i32 s14, 0x1fff
	s_waitcnt lgkmcnt(0)
	v_add_f32_e32 v10, v10, v11
	s_nop 1
	v_mov_b32_dpp v11, v10 row_shl:8 row_mask:0xf bank_mask:0x3
	v_mov_b32_dpp v11, v10 row_shr:8 row_mask:0xf bank_mask:0xc
	s_waitcnt lgkmcnt(0)
	v_add_f32_e32 v10, v10, v11
	ds_bpermute_b32 v11, v43, v10
	s_waitcnt lgkmcnt(0)
	v_add_f32_e32 v12, v10, v11
	v_mul_f32_e32 v10, v31, v31
	v_pk_fma_f32 v[10:11], v[30:31], v[30:31], v[10:11] op_sel_hi:[1,1,0]
	s_nop 1
	v_mov_b32_dpp v15, v10 quad_perm:[1,0,3,2] row_mask:0xf bank_mask:0xf
	v_mov_b32_e32 v17, v10
	ds_bpermute_b32 v13, v44, v12
	s_waitcnt lgkmcnt(0)
	v_pk_add_f32 v[10:11], v[16:17], v[14:15]
	s_nop 1
	v_mov_b32_dpp v15, v11 quad_perm:[2,3,0,1] row_mask:0xf bank_mask:0xf
	s_nop 1
	v_mov_b32_dpp v14, v10 quad_perm:[2,3,0,1] row_mask:0xf bank_mask:0xf
	s_waitcnt lgkmcnt(0)
	v_pk_add_f32 v[10:11], v[10:11], v[14:15]
	s_nop 1
	v_mov_b32_dpp v15, v11 row_shl:4 row_mask:0xf bank_mask:0x5
	v_mov_b32_dpp v15, v11 row_shr:4 row_mask:0xf bank_mask:0xa
	s_nop 1
	v_mov_b32_dpp v14, v10 row_shl:4 row_mask:0xf bank_mask:0x5
	v_mov_b32_dpp v14, v10 row_shr:4 row_mask:0xf bank_mask:0xa
	s_waitcnt lgkmcnt(0)
	v_pk_add_f32 v[10:11], v[10:11], v[14:15]
	s_nop 1
	v_mov_b32_dpp v15, v11 row_shl:8 row_mask:0xf bank_mask:0x3
	v_mov_b32_dpp v15, v11 row_shr:8 row_mask:0xf bank_mask:0xc
	s_nop 1
	v_mov_b32_dpp v14, v10 row_shl:8 row_mask:0xf bank_mask:0x3
	v_mov_b32_dpp v14, v10 row_shr:8 row_mask:0xf bank_mask:0xc
	s_waitcnt lgkmcnt(0)
	v_pk_add_f32 v[10:11], v[10:11], v[14:15]
	v_mov_b32_e32 v15, v11
	s_nop 1
	v_permlane16_swap_b32_e32 v11, v15
	v_mov_b32_e32 v14, v10
	s_nop 1
	v_permlane16_swap_b32_e32 v10, v14
	s_waitcnt lgkmcnt(0)
	v_pk_add_f32 v[10:11], v[10:11], v[14:15]
	ds_bpermute_b32 v15, v44, v11
	v_mov_b32_e32 v14, v10
	s_nop 1
	v_permlane32_swap_b32_e32 v10, v14
	s_waitcnt lgkmcnt(0)
	v_pk_add_f32 v[10:11], v[10:11], v[14:15]
	s_nop 0
	v_pk_fma_f32 v[10:11], v[10:11], s[10:11], v[196:197] op_sel_hi:[1,1,0]
	s_nop 0
	v_cmp_gt_f32_e32 vcc, s95, v10
	v_mul_f32_e32 v14, 0x4b800000, v10
	v_cmp_gt_f32_e64 s[10:11], s95, v11
	v_cndmask_b32_e32 v10, v10, v14, vcc
	v_rsq_f32_e32 v10, v10
	s_nop 0
	v_mul_f32_e32 v14, 0x45800000, v10
	v_cndmask_b32_e32 v10, v10, v14, vcc
	v_mul_f32_e32 v10, v48, v10
	v_mul_f32_e32 v10, v23, v10
	s_nop 1
	v_mov_b32_dpp v14, v10 row_shl:8 row_mask:0xf bank_mask:0x3
	v_mov_b32_dpp v14, v10 row_shr:8 row_mask:0xf bank_mask:0xc
	s_cbranch_scc1 .LBB0_415
	s_and_b32 s15, s14, 63
	s_ashr_i32 s14, s14, 6
	v_mov_b32_e32 v15, s15
	v_mov_b32_e32 v16, s14
	v_cndmask_b32_e64 v15, v15, v16, s[6:7]
	v_lshl_or_b32 v16, v15, 3, v46
	v_ashrrev_i32_e32 v17, 31, v16
	v_lshl_add_u64 v[16:17], v[16:17], 3, s[26:27]
	global_load_dwordx2 v[16:17], v[16:17], off
	s_waitcnt vmcnt(0) lgkmcnt(0)
	v_mul_f32_e32 v14, v17, v14
	v_cndmask_b32_e64 v14, v14, -v14, s[8:9]
	v_fmac_f32_e32 v14, v10, v16
	v_mov_b32_e32 v10, v14
